# adds: expert-weight conversion rewritten by hand around LDS-DMA (two padded LDS slots per wave, conflict-free transposed reads)
# speedup vs baseline: 1.0077x; 1.0077x over previous
.LBB0_1498:
	v_readlane_b32 s7, v249, 16
	s_mov_b32 s27, s53
	s_nop 0
	s_add_i32 s25, s24, s7
	s_cmp_ge_i32 s25, s27
	s_cbranch_scc1 .LBB0_1759
	v_and_b32_e32 v36, 63, v0
	v_lshrrev_b32_e32 v37, 3, v36
	v_and_b32_e32 v38, 7, v36
	v_lshlrev_b32_e32 v38, 4, v38
	v_lshl_add_u32 v82, v37, 11, v38
	v_lshl_add_u32 v83, v37, 13, v38
	v_and_b32_e32 v37, 3, v36
	v_lshrrev_b32_e32 v38, 2, v36
	v_mul_u32_u24_e32 v84, 0x820, v37
	v_lshl_add_u32 v84, v38, 2, v84
	v_lshlrev_b32_e32 v85, 4, v37
	v_lshl_add_u32 v86, v38, 11, v85
	v_lshl_add_u32 v87, v38, 9, v85
	v_mov_b32_e32 v100, 0x42800000
	v_mov_b32_e32 v101, 0x42800000
	v_readlane_b32 s8, v249, 1
	v_readlane_b32 s9, v249, 2
	s_lshl_b32 s72, s7, 1
	s_mul_i32 s72, s72, 8320
	s_add_i32 s86, s72, 8320
	s_cmp_eq_u32 s7, 7
	s_cselect_b32 s86, 0x24000, s86
	s_load_dwordx2 s[10:11], s[8:9], 0xe0
	s_mov_b32 s32, 0
	s_waitcnt lgkmcnt(0)
	s_sub_u32 s7, s25, 0x3e90
	s_lshr_b32 vcc_lo, s7, 15
	s_and_b32 s7, s7, 0x7fff
	s_lshl_b32 vcc_hi, vcc_lo, 3
	s_addk_i32 vcc_hi, 0xa8
	s_load_dwordx2 s[70:71], s[8:9], vcc_hi
	s_lshr_b32 vcc_hi, s7, 9
	s_and_b32 s7, s7, 0x1ff
	s_cmp_eq_u32 vcc_lo, 2
	s_cbranch_scc1 .Lcvda_pdn
	s_lshr_b32 s13, s7, 4
	s_and_b32 s7, s7, 15
	s_lshl_b32 s100, vcc_hi, 21
	s_lshl_b32 s101, vcc_hi, 22
	s_lshl_b32 vcc_hi, s13, 6
	s_add_u32 s100, s100, vcc_hi
	s_lshl_b32 vcc_hi, s13, 17
	s_add_u32 s101, s101, vcc_hi
	s_lshl_b32 vcc_hi, s7, 7
	s_add_u32 s101, s101, vcc_hi
	s_lshr_b32 vcc_hi, s7, 2
	s_lshl_b32 vcc_hi, vcc_hi, 19
	s_add_u32 s100, s100, vcc_hi
	s_and_b32 vcc_hi, s7, 3
	s_lshl_b32 vcc_hi, vcc_hi, 16
	s_add_u32 s100, s100, vcc_hi
	s_lshl_b32 vcc_hi, vcc_lo, 18
	s_add_u32 s100, s100, vcc_hi
	s_add_u32 s100, s100, 0x1b000000
	s_mov_b32 s61, 0x4000
	s_mov_b32 s99, 0
	s_branch .Lcvda_pdd
.Lcvda_pdn:
	s_lshr_b32 s13, s7, 6
	s_and_b32 s7, s7, 63
	s_lshl_b32 s100, vcc_hi, 20
	s_lshl_b32 s101, vcc_hi, 22
	s_lshl_b32 vcc_hi, s13, 6
	s_add_u32 s100, s100, vcc_hi
	s_lshl_b32 vcc_hi, s13, 19
	s_add_u32 s101, s101, vcc_hi
	s_lshl_b32 vcc_hi, s7, 7
	s_add_u32 s101, s101, vcc_hi
	s_lshl_b32 vcc_hi, s7, 14
	s_add_u32 s100, s100, vcc_hi
	s_add_u32 s100, s100, 0x2000000
	s_mov_b32 s61, 0x10000
	s_mov_b32 s99, 1
.Lcvda_pdd:
	s_waitcnt lgkmcnt(0)
	s_add_u32 s70, s70, s101
	s_addc_u32 s71, s71, 0
	s_add_u32 s100, s10, s100
	s_addc_u32 s101, s11, 0
	s_mov_b32 m0, s72
	s_cmp_eq_u32 s99, 0
	s_cbranch_scc0 .Lcvda_pib
	global_load_lds_dwordx4 v82, s[70:71] nt
	s_add_i32 m0, m0, 1040
	s_add_u32 s70, s70, s61
	s_addc_u32 s71, s71, 0
	global_load_lds_dwordx4 v82, s[70:71] nt
	s_add_i32 m0, m0, 1040
	s_add_u32 s70, s70, s61
	s_addc_u32 s71, s71, 0
	global_load_lds_dwordx4 v82, s[70:71] nt
	s_add_i32 m0, m0, 1040
	s_add_u32 s70, s70, s61
	s_addc_u32 s71, s71, 0
	global_load_lds_dwordx4 v82, s[70:71] nt
	s_add_i32 m0, m0, 1040
	s_add_u32 s70, s70, s61
	s_addc_u32 s71, s71, 0
	global_load_lds_dwordx4 v82, s[70:71] nt
	s_add_i32 m0, m0, 1040
	s_add_u32 s70, s70, s61
	s_addc_u32 s71, s71, 0
	global_load_lds_dwordx4 v82, s[70:71] nt
	s_add_i32 m0, m0, 1040
	s_add_u32 s70, s70, s61
	s_addc_u32 s71, s71, 0
	global_load_lds_dwordx4 v82, s[70:71] nt
	s_add_i32 m0, m0, 1040
	s_add_u32 s70, s70, s61
	s_addc_u32 s71, s71, 0
	global_load_lds_dwordx4 v82, s[70:71] nt
	s_branch .Lcvda_pid
.Lcvda_pib:
	global_load_lds_dwordx4 v83, s[70:71] nt
	s_add_i32 m0, m0, 1040
	s_add_u32 s70, s70, s61
	s_addc_u32 s71, s71, 0
	global_load_lds_dwordx4 v83, s[70:71] nt
	s_add_i32 m0, m0, 1040
	s_add_u32 s70, s70, s61
	s_addc_u32 s71, s71, 0
	global_load_lds_dwordx4 v83, s[70:71] nt
	s_add_i32 m0, m0, 1040
	s_add_u32 s70, s70, s61
	s_addc_u32 s71, s71, 0
	global_load_lds_dwordx4 v83, s[70:71] nt
	s_add_i32 m0, m0, 1040
	s_add_u32 s70, s70, s61
	s_addc_u32 s71, s71, 0
	global_load_lds_dwordx4 v83, s[70:71] nt
	s_add_i32 m0, m0, 1040
	s_add_u32 s70, s70, s61
	s_addc_u32 s71, s71, 0
	global_load_lds_dwordx4 v83, s[70:71] nt
	s_add_i32 m0, m0, 1040
	s_add_u32 s70, s70, s61
	s_addc_u32 s71, s71, 0
	global_load_lds_dwordx4 v83, s[70:71] nt
	s_add_i32 m0, m0, 1040
	s_add_u32 s70, s70, s61
	s_addc_u32 s71, s71, 0
	global_load_lds_dwordx4 v83, s[70:71] nt
.Lcvda_pid:
.Lcvda_loop:
	s_mov_b64 s[84:85], s[100:101]
	s_mov_b32 s98, s99
	s_add_i32 s12, s25, 8
	s_cmp_lt_i32 s12, s27
	s_cbranch_scc0 .Lcvda_last
	s_sub_u32 s7, s12, 0x3e90
	s_lshr_b32 vcc_lo, s7, 15
	s_and_b32 s7, s7, 0x7fff
	s_lshl_b32 vcc_hi, vcc_lo, 3
	s_addk_i32 vcc_hi, 0xa8
	s_load_dwordx2 s[70:71], s[8:9], vcc_hi
	s_lshr_b32 vcc_hi, s7, 9
	s_and_b32 s7, s7, 0x1ff
	s_cmp_eq_u32 vcc_lo, 2
	s_cbranch_scc1 .Lcvda_ndn
	s_lshr_b32 s13, s7, 4
	s_and_b32 s7, s7, 15
	s_lshl_b32 s100, vcc_hi, 21
	s_lshl_b32 s101, vcc_hi, 22
	s_lshl_b32 vcc_hi, s13, 6
	s_add_u32 s100, s100, vcc_hi
	s_lshl_b32 vcc_hi, s13, 17
	s_add_u32 s101, s101, vcc_hi
	s_lshl_b32 vcc_hi, s7, 7
	s_add_u32 s101, s101, vcc_hi
	s_lshr_b32 vcc_hi, s7, 2
	s_lshl_b32 vcc_hi, vcc_hi, 19
	s_add_u32 s100, s100, vcc_hi
	s_and_b32 vcc_hi, s7, 3
	s_lshl_b32 vcc_hi, vcc_hi, 16
	s_add_u32 s100, s100, vcc_hi
	s_lshl_b32 vcc_hi, vcc_lo, 18
	s_add_u32 s100, s100, vcc_hi
	s_add_u32 s100, s100, 0x1b000000
	s_mov_b32 s61, 0x4000
	s_mov_b32 s99, 0
	s_branch .Lcvda_ndd

.Lcvda_ndd:
	s_waitcnt lgkmcnt(0)
	s_add_u32 s70, s70, s101
	s_addc_u32 s71, s71, 0
	s_add_u32 s100, s10, s100
	s_addc_u32 s101, s11, 0
	s_mov_b32 m0, s86
	s_cmp_eq_u32 s99, 0
	s_cbranch_scc0 .Lcvda_nib
	global_load_lds_dwordx4 v82, s[70:71] nt
	s_add_i32 m0, m0, 1040
	s_add_u32 s70, s70, s61
	s_addc_u32 s71, s71, 0
	global_load_lds_dwordx4 v82, s[70:71] nt
	s_add_i32 m0, m0, 1040
	s_add_u32 s70, s70, s61
	s_addc_u32 s71, s71, 0
	global_load_lds_dwordx4 v82, s[70:71] nt
	s_add_i32 m0, m0, 1040
	s_add_u32 s70, s70, s61
	s_addc_u32 s71, s71, 0
	global_load_lds_dwordx4 v82, s[70:71] nt
	s_add_i32 m0, m0, 1040
	s_add_u32 s70, s70, s61
	s_addc_u32 s71, s71, 0
	global_load_lds_dwordx4 v82, s[70:71] nt
	s_add_i32 m0, m0, 1040
	s_add_u32 s70, s70, s61
	s_addc_u32 s71, s71, 0
	global_load_lds_dwordx4 v82, s[70:71] nt
	s_add_i32 m0, m0, 1040
	s_add_u32 s70, s70, s61
	s_addc_u32 s71, s71, 0
	global_load_lds_dwordx4 v82, s[70:71] nt
	s_add_i32 m0, m0, 1040
	s_add_u32 s70, s70, s61
	s_addc_u32 s71, s71, 0
	global_load_lds_dwordx4 v82, s[70:71] nt
	s_branch .Lcvda_nid

.Lcvda_nid:
	s_cmp_eq_u32 s32, 0
	s_cbranch_scc1 .Lcvda_w8
	s_waitcnt vmcnt(10)
	s_mov_b32 s13, 1
	s_branch .Lcvda_go
.Lcvda_w8:
	s_waitcnt vmcnt(8)
	s_mov_b32 s13, 1
	s_branch .Lcvda_go
.Lcvda_last:
	s_mov_b32 s13, 0
	s_cmp_eq_u32 s32, 0
	s_cbranch_scc1 .Lcvda_w0
	s_waitcnt vmcnt(2)
	s_branch .Lcvda_go

.Lcvda_go:
	v_add_u32_e32 v89, s72, v84
	v_add_u32_e32 v90, 1040, v89
	ds_read2_b32 v[4:5], v89 offset0:0 offset1:32
	ds_read2_b32 v[6:7], v89 offset0:64 offset1:96
	ds_read2_b32 v[8:9], v89 offset0:128 offset1:160
	ds_read2_b32 v[10:11], v89 offset0:192 offset1:224
	ds_read2_b32 v[12:13], v90 offset0:0 offset1:32
	ds_read2_b32 v[14:15], v90 offset0:64 offset1:96
	ds_read2_b32 v[16:17], v90 offset0:128 offset1:160
	ds_read2_b32 v[18:19], v90 offset0:192 offset1:224
	ds_read2_b32 v[20:21], v89 offset0:16 offset1:48
	ds_read2_b32 v[22:23], v89 offset0:80 offset1:112
	ds_read2_b32 v[24:25], v89 offset0:144 offset1:176
	ds_read2_b32 v[26:27], v89 offset0:208 offset1:240
	ds_read2_b32 v[28:29], v90 offset0:16 offset1:48
	ds_read2_b32 v[30:31], v90 offset0:80 offset1:112
	ds_read2_b32 v[32:33], v90 offset0:144 offset1:176
	ds_read2_b32 v[34:35], v90 offset0:208 offset1:240
	s_cmp_eq_u32 s98, 0
	s_cselect_b64 vcc, -1, 0
	s_movk_i32 s7, 0x2000
	s_cselect_b32 s7, 0x8000, s7
	v_cndmask_b32_e32 v91, v87, v86, vcc
	s_waitcnt lgkmcnt(8)
	v_pk_mul_f32 v[4:5], v[4:5], v[100:101]
	v_pk_mul_f32 v[6:7], v[6:7], v[100:101]
	v_pk_mul_f32 v[8:9], v[8:9], v[100:101]
	v_pk_mul_f32 v[10:11], v[10:11], v[100:101]
	v_pk_mul_f32 v[12:13], v[12:13], v[100:101]
	v_pk_mul_f32 v[14:15], v[14:15], v[100:101]
	v_pk_mul_f32 v[16:17], v[16:17], v[100:101]
	v_pk_mul_f32 v[18:19], v[18:19], v[100:101]
	v_cvt_pk_fp8_f32 v92, v4, v5
	v_cvt_pk_fp8_f32 v93, v8, v9
	v_cvt_pk_fp8_f32 v94, v12, v13
	v_cvt_pk_fp8_f32 v95, v16, v17
	v_cvt_pk_fp8_f32 v92, v6, v7 op_sel:[0,0,1]
	v_cvt_pk_fp8_f32 v93, v10, v11 op_sel:[0,0,1]
	v_cvt_pk_fp8_f32 v94, v14, v15 op_sel:[0,0,1]
	v_cvt_pk_fp8_f32 v95, v18, v19 op_sel:[0,0,1]
	global_store_dwordx4 v91, v[92:95], s[84:85]
	s_waitcnt lgkmcnt(0)
	v_pk_mul_f32 v[20:21], v[20:21], v[100:101]
	v_pk_mul_f32 v[22:23], v[22:23], v[100:101]
	v_pk_mul_f32 v[24:25], v[24:25], v[100:101]
	v_pk_mul_f32 v[26:27], v[26:27], v[100:101]
	v_pk_mul_f32 v[28:29], v[28:29], v[100:101]
	v_pk_mul_f32 v[30:31], v[30:31], v[100:101]
	v_pk_mul_f32 v[32:33], v[32:33], v[100:101]
	v_pk_mul_f32 v[34:35], v[34:35], v[100:101]
	v_cvt_pk_fp8_f32 v96, v20, v21
	v_cvt_pk_fp8_f32 v97, v24, v25
	v_cvt_pk_fp8_f32 v98, v28, v29
	v_cvt_pk_fp8_f32 v99, v32, v33
	v_cvt_pk_fp8_f32 v96, v22, v23 op_sel:[0,0,1]
	v_cvt_pk_fp8_f32 v97, v26, v27 op_sel:[0,0,1]
	v_cvt_pk_fp8_f32 v98, v30, v31 op_sel:[0,0,1]
	v_cvt_pk_fp8_f32 v99, v34, v35 op_sel:[0,0,1]
	s_add_u32 s84, s84, s7
	s_addc_u32 s85, s85, 0
	global_store_dwordx4 v91, v[96:99], s[84:85]
	s_mov_b32 s32, 1
	s_cmp_eq_u32 s13, 0
	s_cbranch_scc1 .LBB0_1759
	s_mov_b32 s25, s12
	s_mov_b32 s7, s72
	s_mov_b32 s72, s86
	s_mov_b32 s86, s7
	s_branch .Lcvda_loop

.LBB0_2595:
	v_readlane_b32 s7, v249, 16
	s_mov_b32 s27, s26
	s_nop 0
	s_add_i32 s25, s6, s7
	s_cmp_ge_i32 s25, s27
	s_cbranch_scc1 .LBB0_2335
	v_and_b32_e32 v36, 63, v0
	v_lshrrev_b32_e32 v37, 3, v36
	v_and_b32_e32 v38, 7, v36
	v_lshlrev_b32_e32 v38, 4, v38
	v_lshl_add_u32 v82, v37, 11, v38
	v_lshl_add_u32 v83, v37, 13, v38
	v_and_b32_e32 v37, 3, v36
	v_lshrrev_b32_e32 v38, 2, v36
	v_mul_u32_u24_e32 v84, 0x820, v37
	v_lshl_add_u32 v84, v38, 2, v84
	v_lshlrev_b32_e32 v85, 4, v37
	v_lshl_add_u32 v86, v38, 11, v85
	v_lshl_add_u32 v87, v38, 9, v85
	v_mov_b32_e32 v100, 0x42800000
	v_mov_b32_e32 v101, 0x42800000
	v_readlane_b32 s8, v249, 1
	v_readlane_b32 s9, v249, 2
	s_lshl_b32 s72, s7, 1
	s_mul_i32 s72, s72, 8320
	s_add_i32 s86, s72, 8320
	s_cmp_eq_u32 s7, 7
	s_cselect_b32 s86, 0x24000, s86
	s_load_dwordx2 s[10:11], s[8:9], 0xe0
	s_mov_b32 s32, 0
	s_waitcnt lgkmcnt(0)
	s_sub_u32 s7, s25, 0x3e90
	s_lshr_b32 vcc_lo, s7, 15
	s_and_b32 s7, s7, 0x7fff
	s_lshl_b32 vcc_hi, vcc_lo, 3
	s_addk_i32 vcc_hi, 0xa8
	s_load_dwordx2 s[70:71], s[8:9], vcc_hi
	s_lshr_b32 vcc_hi, s7, 9
	s_and_b32 s7, s7, 0x1ff
	s_cmp_eq_u32 vcc_lo, 2
	s_cbranch_scc1 .Lcvdb_pdn
	s_lshr_b32 s13, s7, 4
	s_and_b32 s7, s7, 15
	s_lshl_b32 s100, vcc_hi, 21
	s_lshl_b32 s101, vcc_hi, 22
	s_lshl_b32 vcc_hi, s13, 6
	s_add_u32 s100, s100, vcc_hi
	s_lshl_b32 vcc_hi, s13, 17
	s_add_u32 s101, s101, vcc_hi
	s_lshl_b32 vcc_hi, s7, 7
	s_add_u32 s101, s101, vcc_hi
	s_lshr_b32 vcc_hi, s7, 2
	s_lshl_b32 vcc_hi, vcc_hi, 19
	s_add_u32 s100, s100, vcc_hi
	s_and_b32 vcc_hi, s7, 3
	s_lshl_b32 vcc_hi, vcc_hi, 16
	s_add_u32 s100, s100, vcc_hi
	s_lshl_b32 vcc_hi, vcc_lo, 18
	s_add_u32 s100, s100, vcc_hi
	s_add_u32 s100, s100, 0x1b000000
	s_mov_b32 s61, 0x4000
	s_mov_b32 s99, 0
	s_branch .Lcvdb_pdd

.LBB0_2985:
	v_readlane_b32 s7, v249, 16
	s_mov_b32 s27, s23
	s_nop 0
	s_add_i32 s25, s58, s7
	s_cmp_ge_i32 s25, s27
	s_cbranch_scc1 .LBB0_2858
	v_and_b32_e32 v36, 63, v0
	v_lshrrev_b32_e32 v37, 3, v36
	v_and_b32_e32 v38, 7, v36
	v_lshlrev_b32_e32 v38, 4, v38
	v_lshl_add_u32 v82, v37, 11, v38
	v_lshl_add_u32 v83, v37, 13, v38
	v_and_b32_e32 v37, 3, v36
	v_lshrrev_b32_e32 v38, 2, v36
	v_mul_u32_u24_e32 v84, 0x820, v37
	v_lshl_add_u32 v84, v38, 2, v84
	v_lshlrev_b32_e32 v85, 4, v37
	v_lshl_add_u32 v86, v38, 11, v85
	v_lshl_add_u32 v87, v38, 9, v85
	v_mov_b32_e32 v100, 0x42800000
	v_mov_b32_e32 v101, 0x42800000
	v_readlane_b32 s8, v249, 1
	v_readlane_b32 s9, v249, 2
	s_lshl_b32 s72, s7, 1
	s_mul_i32 s72, s72, 8320
	s_add_i32 s86, s72, 8320
	s_cmp_eq_u32 s7, 7
	s_cselect_b32 s86, 0x24000, s86
	s_load_dwordx2 s[10:11], s[8:9], 0xe0
	s_mov_b32 s32, 0
	s_waitcnt lgkmcnt(0)
	s_sub_u32 s7, s25, 0x3e90
	s_lshr_b32 vcc_lo, s7, 15
	s_and_b32 s7, s7, 0x7fff
	s_lshl_b32 vcc_hi, vcc_lo, 3
	s_addk_i32 vcc_hi, 0xa8
	s_load_dwordx2 s[70:71], s[8:9], vcc_hi
	s_lshr_b32 vcc_hi, s7, 9
	s_and_b32 s7, s7, 0x1ff
	s_cmp_eq_u32 vcc_lo, 2
	s_cbranch_scc1 .Lcvdc_pdn
	s_lshr_b32 s13, s7, 4
	s_and_b32 s7, s7, 15
	s_lshl_b32 s100, vcc_hi, 21
	s_lshl_b32 s101, vcc_hi, 22
	s_lshl_b32 vcc_hi, s13, 6
	s_add_u32 s100, s100, vcc_hi
	s_lshl_b32 vcc_hi, s13, 17
	s_add_u32 s101, s101, vcc_hi
	s_lshl_b32 vcc_hi, s7, 7
	s_add_u32 s101, s101, vcc_hi
	s_lshr_b32 vcc_hi, s7, 2
	s_lshl_b32 vcc_hi, vcc_hi, 19
	s_add_u32 s100, s100, vcc_hi
	s_and_b32 vcc_hi, s7, 3
	s_lshl_b32 vcc_hi, vcc_hi, 16
	s_add_u32 s100, s100, vcc_hi
	s_lshl_b32 vcc_hi, vcc_lo, 18
	s_add_u32 s100, s100, vcc_hi
	s_add_u32 s100, s100, 0x1b000000
	s_mov_b32 s61, 0x4000
	s_mov_b32 s99, 0
	s_branch .Lcvdc_pdd

	.amdhsa_kernel _Z8mega_fwd4Args
		.amdhsa_group_segment_fixed_size 16384
		.amdhsa_private_segment_fixed_size 0
		.amdhsa_kernarg_size 504
		.amdhsa_user_sgpr_count 2
		.amdhsa_user_sgpr_dispatch_ptr 0
		.amdhsa_user_sgpr_queue_ptr 0
		.amdhsa_user_sgpr_kernarg_segment_ptr 1
		.amdhsa_user_sgpr_dispatch_id 0
		.amdhsa_user_sgpr_kernarg_preload_length 0
		.amdhsa_user_sgpr_kernarg_preload_offset 0
		.amdhsa_user_sgpr_private_segment_size 0
		.amdhsa_uses_dynamic_stack 0
		.amdhsa_enable_private_segment 0
		.amdhsa_system_sgpr_workgroup_id_x 1
		.amdhsa_system_sgpr_workgroup_id_y 0
		.amdhsa_system_sgpr_workgroup_id_z 0
		.amdhsa_system_sgpr_workgroup_info 0
		.amdhsa_system_vgpr_workitem_id 0
		.amdhsa_next_free_vgpr 250
		.amdhsa_next_free_sgpr 102
		.amdhsa_accum_offset 252
		.amdhsa_reserve_vcc 1
		.amdhsa_float_round_mode_32 0
		.amdhsa_float_round_mode_16_64 0
		.amdhsa_float_denorm_mode_32 3
		.amdhsa_float_denorm_mode_16_64 3
		.amdhsa_dx10_clamp 1
		.amdhsa_ieee_mode 1
		.amdhsa_fp16_overflow 0
		.amdhsa_tg_split 0
		.amdhsa_exception_fp_ieee_invalid_op 0
		.amdhsa_exception_fp_denorm_src 0
		.amdhsa_exception_fp_ieee_div_zero 0
		.amdhsa_exception_fp_ieee_overflow 0
		.amdhsa_exception_fp_ieee_underflow 0
		.amdhsa_exception_fp_ieee_inexact 0
		.amdhsa_exception_int_div_zero 0
	.end_amdhsa_kernel

amdhsa.kernels:
  - .agpr_count:     0
    .args:
      - .offset:         0
        .size:           248
        .value_kind:     by_value
      - .offset:         248
        .size:           4
        .value_kind:     hidden_block_count_x
      - .offset:         252
        .size:           4
        .value_kind:     hidden_block_count_y
      - .offset:         256
        .size:           4
        .value_kind:     hidden_block_count_z
      - .offset:         260
        .size:           2
        .value_kind:     hidden_group_size_x
      - .offset:         262
        .size:           2
        .value_kind:     hidden_group_size_y
      - .offset:         264
        .size:           2
        .value_kind:     hidden_group_size_z
      - .offset:         266
        .size:           2
        .value_kind:     hidden_remainder_x
      - .offset:         268
        .size:           2
        .value_kind:     hidden_remainder_y
      - .offset:         270
        .size:           2
        .value_kind:     hidden_remainder_z
      - .offset:         288
        .size:           8
        .value_kind:     hidden_global_offset_x
      - .offset:         296
        .size:           8
        .value_kind:     hidden_global_offset_y
      - .offset:         304
        .size:           8
        .value_kind:     hidden_global_offset_z
      - .offset:         312
        .size:           2
        .value_kind:     hidden_grid_dims
      - .offset:         368
        .size:           4
        .value_kind:     hidden_dynamic_lds_size
    .group_segment_fixed_size: 16384
    .kernarg_segment_align: 8
    .kernarg_segment_size: 504
    .language:       OpenCL C
    .language_version:
      - 2
      - 0
    .max_flat_workgroup_size: 512
    .name:           _Z8mega_fwd4Args
    .private_segment_fixed_size: 0
    .sgpr_count:     108
    .sgpr_spill_count: 295
    .symbol:         _Z8mega_fwd4Args.kd
    .uniform_work_group_size: 1
    .uses_dynamic_stack: false
    .vgpr_count:     250
    .vgpr_spill_count: 0
    .wavefront_size: 64
